# mlp late loads hoisted; pool2 A-fragment LDS reads as 2x ds_read_b128 (bank conflicts)
# speedup vs baseline: 1.0492x; 1.0172x over previous
.LBB4_35:
	s_or_b64 exec, exec, s[0:1]
	v_lshlrev_b32_e32 v66, 4, v93
	v_and_b32_e32 v66, 48, v66
	v_or_b32_e32 v67, v66, v90
	v_mul_u32_u24_e32 v67, 0x210, v67
	v_lshlrev_b32_e32 v68, 5, v1
	v_add3_u32 v67, v99, v67, v68
	s_waitcnt lgkmcnt(0)
	s_barrier
	ds_read_b128 v[96:99], v67
	ds_read_b128 v[100:103], v67 offset:16
	ds_read_b128 v[104:107], v67 offset:128
	ds_read_b128 v[108:111], v67 offset:144
	ds_read_b128 v[112:115], v67 offset:256
	ds_read_b128 v[116:119], v67 offset:272
	ds_read_b128 v[120:123], v67 offset:384
	ds_read_b128 v[124:127], v67 offset:400
	s_movk_i32 s0, 0x200
	v_cmp_gt_u32_e32 vcc, s0, v0
	s_movk_i32 s0, 0x1ff
	v_cmp_lt_u32_e64 s[0:1], s0, v0
	v_lshlrev_b32_e32 v0, 4, v92
	s_waitcnt vmcnt(0)
	s_waitcnt lgkmcnt(6)
	v_cvt_pk_f16_f32 v68, v96, v97
	v_cvt_pk_f16_f32 v69, v98, v99
	v_cvt_pk_f16_f32 v70, v100, v101
	v_cvt_pk_f16_f32 v71, v102, v103
	s_nop 1
	v_mfma_f32_16x16x32_f16 v[2:5], v[68:71], v[2:5], 0
	v_mfma_f32_16x16x32_f16 v[6:9], v[68:71], v[6:9], 0
	v_mfma_f32_16x16x32_f16 v[22:25], v[68:71], v[22:25], 0
	v_mfma_f32_16x16x32_f16 v[10:13], v[68:71], v[10:13], 0
	s_waitcnt lgkmcnt(4)
	v_cvt_pk_f16_f32 v72, v104, v105
	v_cvt_pk_f16_f32 v73, v106, v107
	v_cvt_pk_f16_f32 v74, v108, v109
	v_cvt_pk_f16_f32 v75, v110, v111
	s_nop 1
	v_mfma_f32_16x16x32_f16 v[2:5], v[72:75], v[14:17], v[2:5]
	v_mfma_f32_16x16x32_f16 v[6:9], v[72:75], v[18:21], v[6:9]
	v_mfma_f32_16x16x32_f16 v[14:17], v[72:75], v[62:65], v[22:25]
	v_mfma_f32_16x16x32_f16 v[10:13], v[72:75], v[58:61], v[10:13]
	s_waitcnt lgkmcnt(2)
	v_cvt_pk_f16_f32 v76, v112, v113
	v_cvt_pk_f16_f32 v77, v114, v115
	v_cvt_pk_f16_f32 v78, v116, v117
	v_cvt_pk_f16_f32 v79, v118, v119
	s_nop 1
	v_mfma_f32_16x16x32_f16 v[22:25], v[76:79], v[54:57], v[14:17]
	v_mfma_f32_16x16x32_f16 v[2:5], v[76:79], v[46:49], v[2:5]
	v_mfma_f32_16x16x32_f16 v[6:9], v[76:79], v[50:53], v[6:9]
	v_mfma_f32_16x16x32_f16 v[18:21], v[76:79], v[42:45], v[10:13]
	s_waitcnt lgkmcnt(0)
	v_cvt_pk_f16_f32 v80, v120, v121
	v_cvt_pk_f16_f32 v81, v122, v123
	v_cvt_pk_f16_f32 v82, v124, v125
	v_cvt_pk_f16_f32 v83, v126, v127
	s_nop 1
	s_barrier
	v_mfma_f32_16x16x32_f16 v[14:17], v[80:83], v[26:29], v[2:5]
	v_mfma_f32_16x16x32_f16 v[10:13], v[80:83], v[30:33], v[6:9]
	v_mfma_f32_16x16x32_f16 v[6:9], v[80:83], v[34:37], v[22:25]
	v_mfma_f32_16x16x32_f16 v[2:5], v[80:83], v[38:41], v[18:21]
	s_and_saveexec_b64 s[4:5], s[0:1]
	s_cbranch_execz .LBB4_37
	s_nop 0
	v_lshl_or_b32 v18, v93, 12, v0
	s_nop 0
	ds_write_b128 v18, v[14:17] offset:33792
	ds_write_b128 v18, v[10:13] offset:34816
	ds_write_b128 v18, v[6:9] offset:35840
	ds_write_b128 v18, v[2:5] offset:36864

	.amdhsa_kernel _Z12pool2_kernelPKjPKiPKfPK15HIP_vector_typeIfLj4EEPKDF16_Pfi
		.amdhsa_group_segment_fixed_size 69728
		.amdhsa_private_segment_fixed_size 0
		.amdhsa_kernarg_size 52
		.amdhsa_user_sgpr_count 2
		.amdhsa_user_sgpr_dispatch_ptr 0
		.amdhsa_user_sgpr_queue_ptr 0
		.amdhsa_user_sgpr_kernarg_segment_ptr 1
		.amdhsa_user_sgpr_dispatch_id 0
		.amdhsa_user_sgpr_kernarg_preload_length 0
		.amdhsa_user_sgpr_kernarg_preload_offset 0
		.amdhsa_user_sgpr_private_segment_size 0
		.amdhsa_uses_dynamic_stack 0
		.amdhsa_enable_private_segment 0
		.amdhsa_system_sgpr_workgroup_id_x 1
		.amdhsa_system_sgpr_workgroup_id_y 0
		.amdhsa_system_sgpr_workgroup_id_z 0
		.amdhsa_system_sgpr_workgroup_info 0
		.amdhsa_system_vgpr_workitem_id 0
		.amdhsa_next_free_vgpr 128
		.amdhsa_next_free_sgpr 20
		.amdhsa_accum_offset 128
		.amdhsa_reserve_vcc 1
		.amdhsa_float_round_mode_32 0
		.amdhsa_float_round_mode_16_64 0
		.amdhsa_float_denorm_mode_32 3
		.amdhsa_float_denorm_mode_16_64 3
		.amdhsa_dx10_clamp 1
		.amdhsa_ieee_mode 1
		.amdhsa_fp16_overflow 0
		.amdhsa_tg_split 0
		.amdhsa_exception_fp_ieee_invalid_op 0
		.amdhsa_exception_fp_denorm_src 0
		.amdhsa_exception_fp_ieee_div_zero 0
		.amdhsa_exception_fp_ieee_overflow 0
		.amdhsa_exception_fp_ieee_underflow 0
		.amdhsa_exception_fp_ieee_inexact 0
		.amdhsa_exception_int_div_zero 0
	.end_amdhsa_kernel

_Z10mlp_kernelPKfPKiS0_S0_S0_S0_S0_S0_Pf:
	s_load_dwordx2 s[4:5], s[0:1], 0x0
	s_load_dwordx2 s[6:7], s[0:1], 0x10
	s_load_dwordx2 s[8:9], s[0:1], 0x20
	s_load_dwordx2 s[34:35], s[0:1], 0x8
	s_load_dwordx2 s[36:37], s[0:1], 0x18
	s_load_dwordx2 s[38:39], s[0:1], 0x28
	s_load_dwordx4 s[40:43], s[0:1], 0x30
	v_and_b32_e32 v1, 0x7f, v0
	v_lshrrev_b32_e32 v33, 7, v0
	v_lshlrev_b32_e32 v4, 2, v1
	v_lshl_or_b32 v2, v33, 13, v4
	v_mov_b32_e32 v3, 0
	s_waitcnt lgkmcnt(0)
	s_lshl_b32 s44, s2, 2
	s_add_u32 s34, s34, s44
	s_addc_u32 s35, s35, 0
	s_load_dword s45, s[34:35], 0x0
	s_load_dword s46, s[34:35], 0x100
	s_load_dword s47, s[34:35], 0x200
	s_load_dword s48, s[34:35], 0x300
	s_load_dword s49, s[34:35], 0x400
	s_load_dword s50, s[34:35], 0x500
	s_load_dword s51, s[34:35], 0x600
	s_load_dword s52, s[34:35], 0x700
	s_load_dword s53, s[34:35], 0x800
	s_load_dword s54, s[34:35], 0x900
	s_load_dword s55, s[34:35], 0xa00
	s_load_dword s56, s[34:35], 0xb00
	s_load_dword s57, s[34:35], 0xc00
	s_load_dword s58, s[34:35], 0xd00
	s_load_dword s59, s[34:35], 0xe00
	s_load_dword s60, s[34:35], 0xf00
	s_load_dword s61, s[34:35], 0x1000
	s_load_dword s62, s[34:35], 0x1100
	s_load_dword s63, s[34:35], 0x1200
	s_load_dword s64, s[34:35], 0x1300
	s_load_dword s65, s[34:35], 0x1400
	s_load_dword s66, s[34:35], 0x1500
	s_load_dword s67, s[34:35], 0x1600
	s_load_dword s68, s[34:35], 0x1700
	s_load_dword s69, s[34:35], 0x1800
	v_min_u32_e32 v64, 0x7f, v0
	v_lshlrev_b32_e32 v64, 2, v64
	global_load_dword v65, v64, s[36:37]
	v_min_u32_e32 v66, 63, v0
	v_lshlrev_b32_e32 v66, 2, v66
	global_load_dword v67, v66, s[38:39]
	v_and_b32_e32 v68, 15, v0
	v_lshrrev_b32_e32 v69, 4, v0
	v_min_u32_e32 v69, 9, v69
	v_mul_u32_u24_e32 v70, 40, v68
	v_add_lshl_u32 v70, v70, v69, 2
	global_load_dword v71, v70, s[40:41]
	global_load_dword v72, v70, s[40:41] offset:40
	global_load_dword v73, v70, s[40:41] offset:80
	global_load_dword v74, v70, s[40:41] offset:120
	v_lshlrev_b32_e32 v75, 2, v69
	global_load_dword v76, v75, s[42:43]
	v_lshl_add_u64 v[6:7], s[6:7], 0, v[2:3]
	global_load_dword v32, v2, s[6:7]
	global_load_dword v30, v2, s[6:7] offset:512
	global_load_dword v28, v2, s[6:7] offset:1024
	global_load_dword v26, v2, s[6:7] offset:1536
	global_load_dword v24, v2, s[6:7] offset:2048
	global_load_dword v22, v2, s[6:7] offset:2560
	global_load_dword v20, v2, s[6:7] offset:3072
	global_load_dword v18, v2, s[6:7] offset:3584
	s_movk_i32 s3, 0x1000
	v_and_b32_e32 v2, 63, v0
	v_add_co_u32_e32 v6, vcc, s3, v6
	v_lshrrev_b32_e32 v1, 6, v0
	v_lshlrev_b32_e32 v8, 2, v2
	v_addc_co_u32_e32 v7, vcc, 0, v7, vcc
	v_lshl_or_b32 v2, v1, 11, v8
	global_load_dword v31, v[6:7], off
	global_load_dword v29, v[6:7], off offset:512
	global_load_dword v27, v[6:7], off offset:1024
	global_load_dword v25, v[6:7], off offset:1536
	global_load_dword v23, v[6:7], off offset:2048
	global_load_dword v21, v[6:7], off offset:2560
	global_load_dword v19, v[6:7], off offset:3072
	global_load_dword v17, v[6:7], off offset:3584
	global_load_dword v16, v2, s[8:9]
	global_load_dword v15, v2, s[8:9] offset:256
	global_load_dword v14, v2, s[8:9] offset:512
	global_load_dword v13, v2, s[8:9] offset:768
	global_load_dword v12, v2, s[8:9] offset:1024
	global_load_dword v11, v2, s[8:9] offset:1280
	global_load_dword v10, v2, s[8:9] offset:1536
	global_load_dword v9, v2, s[8:9] offset:1792
	s_ashr_i32 s3, s2, 31
	v_lshlrev_b32_e32 v2, 6, v33
	v_mov_b32_e32 v5, v3
	v_lshl_add_u64 v[34:35], v[2:3], 0, s[2:3]
	v_lshl_add_u64 v[6:7], s[4:5], 0, v[4:5]
	v_lshlrev_b64 v[34:35], 9, v[34:35]
	v_lshl_add_u64 v[42:43], v[6:7], 0, v[34:35]
	v_or_b32_e32 v34, 0x200, v2
	v_mov_b32_e32 v35, v3
	v_lshl_add_u64 v[34:35], v[34:35], 0, s[2:3]
	v_lshlrev_b64 v[34:35], 9, v[34:35]
	v_lshl_add_u64 v[44:45], v[6:7], 0, v[34:35]
	v_or_b32_e32 v34, 0x400, v2
	v_mov_b32_e32 v35, v3
	v_lshl_add_u64 v[34:35], v[34:35], 0, s[2:3]
	v_lshlrev_b64 v[34:35], 9, v[34:35]
	v_lshl_add_u64 v[46:47], v[6:7], 0, v[34:35]
	v_or_b32_e32 v34, 0x600, v2
	v_mov_b32_e32 v35, v3
	v_lshl_add_u64 v[34:35], v[34:35], 0, s[2:3]
	v_lshlrev_b64 v[34:35], 9, v[34:35]
	v_lshl_add_u64 v[48:49], v[6:7], 0, v[34:35]
	v_or_b32_e32 v34, 0x800, v2
	v_mov_b32_e32 v35, v3
	v_lshl_add_u64 v[34:35], v[34:35], 0, s[2:3]
	v_lshlrev_b64 v[34:35], 9, v[34:35]
	v_lshl_add_u64 v[50:51], v[6:7], 0, v[34:35]
	v_or_b32_e32 v34, 0xa00, v2
	v_mov_b32_e32 v35, v3
	v_lshl_add_u64 v[34:35], v[34:35], 0, s[2:3]
	v_lshlrev_b64 v[34:35], 9, v[34:35]
	v_lshl_add_u64 v[52:53], v[6:7], 0, v[34:35]
	v_or_b32_e32 v34, 0xc00, v2
	v_mov_b32_e32 v35, v3
	v_lshl_add_u64 v[34:35], v[34:35], 0, s[2:3]
	v_lshlrev_b64 v[34:35], 9, v[34:35]
	v_lshl_add_u64 v[54:55], v[6:7], 0, v[34:35]
	v_or_b32_e32 v34, 0xe00, v2
	v_mov_b32_e32 v35, v3
	v_lshl_add_u64 v[34:35], v[34:35], 0, s[2:3]
	v_lshlrev_b64 v[34:35], 9, v[34:35]
	v_lshl_add_u64 v[56:57], v[6:7], 0, v[34:35]
	global_load_dword v5, v[42:43], off
	global_load_dword v34, v[44:45], off
	global_load_dword v35, v[46:47], off
	global_load_dword v36, v[48:49], off
	global_load_dword v37, v[50:51], off
	global_load_dword v38, v[52:53], off
	global_load_dword v39, v[54:55], off
	global_load_dword v40, v[56:57], off
	v_or_b32_e32 v42, 0x1000, v2
	v_mov_b32_e32 v43, v3
	v_lshl_add_u64 v[42:43], v[42:43], 0, s[2:3]
	v_lshlrev_b64 v[42:43], 9, v[42:43]
	v_lshl_add_u64 v[48:49], v[6:7], 0, v[42:43]
	v_or_b32_e32 v42, 0x1200, v2
	v_mov_b32_e32 v43, v3
	v_lshl_add_u64 v[42:43], v[42:43], 0, s[2:3]
	v_lshlrev_b64 v[42:43], 9, v[42:43]
	v_lshl_add_u64 v[50:51], v[6:7], 0, v[42:43]
	v_or_b32_e32 v42, 0x1400, v2
	v_mov_b32_e32 v43, v3
	v_lshl_add_u64 v[42:43], v[42:43], 0, s[2:3]
	v_lshlrev_b64 v[42:43], 9, v[42:43]
	v_lshl_add_u64 v[52:53], v[6:7], 0, v[42:43]
	v_or_b32_e32 v42, 0x1600, v2
	v_mov_b32_e32 v43, v3
	v_lshl_add_u64 v[42:43], v[42:43], 0, s[2:3]
	v_lshlrev_b64 v[42:43], 9, v[42:43]
	v_lshl_add_u64 v[54:55], v[6:7], 0, v[42:43]
	v_or_b32_e32 v42, 0x1800, v2
	v_mov_b32_e32 v43, v3
	v_lshl_add_u64 v[42:43], v[42:43], 0, s[2:3]
	v_lshlrev_b64 v[42:43], 9, v[42:43]
	v_lshl_add_u64 v[56:57], v[6:7], 0, v[42:43]
	v_or_b32_e32 v42, 0x1a00, v2
	v_mov_b32_e32 v43, v3
	v_lshl_add_u64 v[42:43], v[42:43], 0, s[2:3]
	v_lshlrev_b64 v[42:43], 9, v[42:43]
	v_lshl_add_u64 v[58:59], v[6:7], 0, v[42:43]
	v_or_b32_e32 v42, 0x1c00, v2
	v_mov_b32_e32 v43, v3
	v_lshl_add_u64 v[42:43], v[42:43], 0, s[2:3]
	v_lshlrev_b64 v[42:43], 9, v[42:43]
	v_lshl_add_u64 v[60:61], v[6:7], 0, v[42:43]
	v_or_b32_e32 v42, 0x1e00, v2
	v_mov_b32_e32 v43, v3
	v_lshl_add_u64 v[42:43], v[42:43], 0, s[2:3]
	v_lshlrev_b64 v[42:43], 9, v[42:43]
	v_lshl_add_u64 v[62:63], v[6:7], 0, v[42:43]
	global_load_dword v41, v[48:49], off
	global_load_dword v42, v[50:51], off
	global_load_dword v43, v[52:53], off
	global_load_dword v44, v[54:55], off
	global_load_dword v45, v[56:57], off
	global_load_dword v46, v[58:59], off
	global_load_dword v47, v[60:61], off
	global_load_dword v48, v[62:63], off
	v_or_b32_e32 v50, 0x2000, v2
	v_mov_b32_e32 v51, v3
	v_lshl_add_u64 v[50:51], v[50:51], 0, s[2:3]
	v_lshlrev_b64 v[50:51], 9, v[50:51]
	v_lshl_add_u64 v[52:53], v[6:7], 0, v[50:51]
	v_or_b32_e32 v50, 0x2200, v2
	v_mov_b32_e32 v51, v3
	v_lshl_add_u64 v[50:51], v[50:51], 0, s[2:3]
	v_lshlrev_b64 v[50:51], 9, v[50:51]
	v_lshl_add_u64 v[54:55], v[6:7], 0, v[50:51]
	global_load_dword v49, v[52:53], off
	global_load_dword v50, v[54:55], off
	v_or_b32_e32 v52, 0x2400, v2
	v_mov_b32_e32 v53, v3
	v_lshl_add_u64 v[52:53], v[52:53], 0, s[2:3]
	v_lshlrev_b64 v[52:53], 9, v[52:53]
	v_lshl_add_u64 v[56:57], v[6:7], 0, v[52:53]
	v_or_b32_e32 v52, 0x2600, v2
	v_mov_b32_e32 v53, v3
	v_lshl_add_u64 v[52:53], v[52:53], 0, s[2:3]
	v_lshlrev_b64 v[52:53], 9, v[52:53]
	v_lshl_add_u64 v[58:59], v[6:7], 0, v[52:53]
	v_or_b32_e32 v52, 0x2800, v2
	v_mov_b32_e32 v53, v3
	v_lshl_add_u64 v[52:53], v[52:53], 0, s[2:3]
	v_lshlrev_b64 v[52:53], 9, v[52:53]
	v_lshl_add_u64 v[60:61], v[6:7], 0, v[52:53]
	v_or_b32_e32 v52, 0x2a00, v2
	v_mov_b32_e32 v53, v3
	v_lshl_add_u64 v[52:53], v[52:53], 0, s[2:3]
	v_lshlrev_b64 v[52:53], 9, v[52:53]
	v_lshl_add_u64 v[62:63], v[6:7], 0, v[52:53]
	global_load_dword v51, v[56:57], off
	global_load_dword v52, v[58:59], off
	global_load_dword v53, v[60:61], off
	global_load_dword v54, v[62:63], off
	v_or_b32_e32 v56, 0x2c00, v2
	v_mov_b32_e32 v57, v3
	v_lshl_add_u64 v[56:57], v[56:57], 0, s[2:3]
	v_lshlrev_b64 v[56:57], 9, v[56:57]
	v_lshl_add_u64 v[58:59], v[6:7], 0, v[56:57]
	v_or_b32_e32 v56, 0x2e00, v2
	v_mov_b32_e32 v57, v3
	v_lshl_add_u64 v[56:57], v[56:57], 0, s[2:3]
	v_lshlrev_b64 v[56:57], 9, v[56:57]
	v_lshl_add_u64 v[60:61], v[6:7], 0, v[56:57]
	global_load_dword v55, v[58:59], off
	global_load_dword v56, v[60:61], off
	v_or_b32_e32 v57, 0xc0, v33
	s_movk_i32 s4, 0xc4
	v_cmp_gt_u32_e32 vcc, s4, v57
	s_and_saveexec_b64 s[4:5], vcc
	s_cbranch_execz .LBB5_2
	v_lshlrev_b32_e32 v58, 6, v57
	v_mov_b32_e32 v59, 0
	v_lshl_add_u64 v[58:59], v[58:59], 0, s[2:3]
	v_lshlrev_b64 v[58:59], 9, v[58:59]
	v_lshl_add_u64 v[6:7], v[6:7], 0, v[58:59]
	global_load_dword v3, v[6:7], off

.LBB5_4:
	s_or_b64 exec, exec, s[4:5]
	s_waitcnt lgkmcnt(0)
	s_barrier
	ds_read_b128 v[34:37], v2 offset:8192
	ds_read_b128 v[38:41], v2 offset:8208
	ds_read_b128 v[42:45], v2 offset:8224
	ds_read_b128 v[46:49], v2 offset:8240
	s_waitcnt lgkmcnt(3)
	v_fma_f32 v2, v34, v32, 0
	v_fmac_f32_e32 v2, v35, v30
	v_fmac_f32_e32 v2, v36, v28
	v_fmac_f32_e32 v2, v37, v26
	s_waitcnt lgkmcnt(2)
	v_fmac_f32_e32 v2, v38, v24
	v_fmac_f32_e32 v2, v39, v22
	v_fmac_f32_e32 v2, v40, v20
	v_fmac_f32_e32 v2, v41, v18
	s_waitcnt lgkmcnt(1)
	v_fmac_f32_e32 v2, v42, v31
	v_fmac_f32_e32 v2, v43, v29
	v_fmac_f32_e32 v2, v44, v27
	v_fmac_f32_e32 v2, v45, v25
	s_waitcnt lgkmcnt(0)
	v_fmac_f32_e32 v2, v46, v23
	v_fmac_f32_e32 v2, v47, v21
	v_fmac_f32_e32 v2, v48, v19
	v_fmac_f32_e32 v2, v49, v17
	ds_write_b32 v4, v2
	s_waitcnt lgkmcnt(0)
	s_barrier
	s_and_saveexec_b64 s[4:5], vcc
	s_cbranch_execz .LBB5_6
	ds_read2st64_b32 v[4:5], v3 offset1:2
	ds_read2st64_b32 v[6:7], v3 offset0:8 offset1:10
	ds_read2st64_b32 v[18:19], v3 offset0:4 offset1:6
	ds_read2st64_b32 v[20:21], v3 offset0:12 offset1:14
	s_waitcnt lgkmcnt(0)
	s_add_i32 s31, s45, s46
	s_add_i32 s31, s31, s47
	s_add_i32 s31, s31, s48
	s_add_i32 s31, s31, s49
	s_add_i32 s31, s31, s50
	s_add_i32 s31, s31, s51
	s_add_i32 s31, s31, s52
	s_add_i32 s31, s31, s53
	s_add_i32 s31, s31, s54
	s_add_i32 s31, s31, s55
	s_add_i32 s31, s31, s56
	s_add_i32 s31, s31, s57
	s_add_i32 s31, s31, s58
	s_add_i32 s31, s31, s59
	s_add_i32 s31, s31, s60
	s_add_i32 s31, s31, s61
	s_add_i32 s31, s31, s62
	s_add_i32 s31, s31, s63
	s_add_i32 s31, s31, s64
	s_add_i32 s31, s31, s65
	s_add_i32 s31, s31, s66
	s_add_i32 s31, s31, s67
	s_add_i32 s31, s31, s68
	s_add_i32 s31, s31, s69
	v_mov_b32_e32 v22, v4
	v_mov_b32_e32 v23, v6
	v_mov_b32_e32 v6, v5
	v_mov_b32_e32 v4, v18
	v_mov_b32_e32 v5, v20
	v_mov_b32_e32 v20, v19
	v_cvt_f32_i32_e32 v17, s31
	v_pk_add_f32 v[6:7], v[22:23], v[6:7]
	v_pk_add_f32 v[4:5], v[4:5], v[20:21]
	s_nop 0
	v_pk_add_f32 v[4:5], v[6:7], v[4:5]
	s_nop 0
	v_add_f32_e32 v4, v4, v5
	v_max_f32_e32 v5, 1.0, v17
	s_waitcnt vmcnt(0)
	v_fmac_f32_e32 v4, v65, v17
	v_div_scale_f32 v2, s[6:7], v5, v5, v4
	v_rcp_f32_e32 v6, v2
	v_div_scale_f32 v7, vcc, v4, v5, v4
	v_fma_f32 v17, -v2, v6, 1.0
	v_fmac_f32_e32 v6, v17, v6
	v_mul_f32_e32 v17, v7, v6
	v_fma_f32 v18, -v2, v17, v7
	v_fmac_f32_e32 v17, v18, v6
	v_fma_f32 v2, -v2, v17, v7
	v_div_fmas_f32 v2, v2, v6, v17
	v_div_fixup_f32 v2, v2, v5, v4
	ds_write_b32 v3, v2 offset:8704
.LBB5_6:
	s_or_b64 exec, exec, s[4:5]
	v_lshlrev_b32_e32 v2, 5, v1
	s_waitcnt lgkmcnt(0)
	s_barrier
	ds_read_b128 v[4:7], v2 offset:8704
	s_load_dwordx2 s[8:9], s[0:1], 0x40
	s_load_dwordx4 s[4:7], s[0:1], 0x30
	ds_read_b128 v[18:21], v2 offset:8720
	v_lshl_or_b32 v1, v1, 8, v8
	v_cmp_gt_u32_e32 vcc, 64, v0
	s_waitcnt lgkmcnt(0)
	v_fma_f32 v2, v4, v16, 0
	v_fmac_f32_e32 v2, v5, v15
	v_fmac_f32_e32 v2, v6, v14
	v_fmac_f32_e32 v2, v7, v13
	v_fmac_f32_e32 v2, v18, v12
	v_fmac_f32_e32 v2, v19, v11
	v_fmac_f32_e32 v2, v20, v10
	v_fmac_f32_e32 v2, v21, v9
	ds_write_b32 v1, v2 offset:4096
	s_waitcnt lgkmcnt(0)
	s_barrier
	s_and_saveexec_b64 s[10:11], vcc
	s_cbranch_execz .LBB5_10
	v_mov_b32_e32 v1, v67
	ds_read2st64_b32 v[4:5], v3 offset0:16 offset1:17
	ds_read2st64_b32 v[6:7], v3 offset0:18 offset1:19
	ds_read2st64_b32 v[8:9], v3 offset0:20 offset1:21
	ds_read2st64_b32 v[10:11], v3 offset0:22 offset1:23
	ds_read2st64_b32 v[12:13], v3 offset0:24 offset1:25
	s_waitcnt vmcnt(0) lgkmcnt(4)
	v_add_f32_e32 v1, v1, v4
	v_add_f32_e32 v1, v1, v5
	s_waitcnt lgkmcnt(3)
	v_add_f32_e32 v1, v1, v6
	v_add_f32_e32 v1, v1, v7
	s_waitcnt lgkmcnt(2)
	v_add_f32_e32 v1, v1, v8
	v_add_f32_e32 v1, v1, v9
	s_waitcnt lgkmcnt(1)
	v_add_f32_e32 v1, v1, v10
	v_add_f32_e32 v1, v1, v11
	ds_read2st64_b32 v[4:5], v3 offset0:26 offset1:27
	ds_read2st64_b32 v[6:7], v3 offset0:28 offset1:29
	ds_read2st64_b32 v[8:9], v3 offset0:30 offset1:31
	s_waitcnt lgkmcnt(3)
	v_add_f32_e32 v1, v1, v12
	v_add_f32_e32 v1, v1, v13
	s_waitcnt lgkmcnt(2)
	v_add_f32_e32 v1, v1, v4
	v_add_f32_e32 v1, v1, v5
	s_waitcnt lgkmcnt(1)
	v_add_f32_e32 v1, v1, v6
	v_add_f32_e32 v1, v1, v7
	s_waitcnt lgkmcnt(0)
	v_add_f32_e32 v1, v1, v8
	v_add_f32_e32 v1, v1, v9
	v_cmp_nlt_f32_e32 vcc, 0, v1
	s_and_saveexec_b64 s[0:1], vcc
	s_cbranch_execz .LBB5_9
	v_mul_f32_e32 v2, 0x3fb8aa3b, v1
	v_rndne_f32_e32 v2, v2
	v_fmamk_f32 v4, v2, 0xbf317218, v1
	v_fmamk_f32 v4, v2, 0x3102e308, v4
	v_mov_b32_e32 v5, 0x3ab69700
	v_fmac_f32_e32 v5, 0x395133b1, v4
	v_fmaak_f32 v5, v4, v5, 0x3c0887f9
	v_fmaak_f32 v5, v4, v5, 0x3d2aaa81
	v_cvt_i32_f32_e32 v6, v2
	v_fmaak_f32 v5, v4, v5, 0x3e2aaaab
	v_fma_f32 v5, v4, v5, 0.5
	v_mul_f32_e32 v5, v4, v5
	s_mov_b32 s3, 0x43000000
	v_fmac_f32_e32 v4, v4, v5
	v_ldexp_f32 v5, 1.0, v6
	v_mov_b32_e32 v6, 0x7f000000
	v_cmp_eq_f32_e32 vcc, s3, v2
	s_mov_b32 s3, 0xc1880000
	s_nop 0
	v_cndmask_b32_e32 v2, v5, v6, vcc
	v_add_f32_e32 v5, -1.0, v2
	v_fmac_f32_e32 v5, v2, v4
	v_add_f32_e32 v2, v5, v5
	v_cndmask_b32_e32 v2, v5, v2, vcc
	v_cmp_ngt_f32_e32 vcc, s3, v1
	s_nop 1
	v_cndmask_b32_e32 v1, -1.0, v2, vcc

.LBB5_10:
	s_or_b64 exec, exec, s[10:11]
	s_movk_i32 s0, 0xa0
	v_cmp_gt_u32_e32 vcc, s0, v0
	s_waitcnt lgkmcnt(0)
	s_barrier
	s_and_saveexec_b64 s[0:1], vcc
	s_cbranch_execz .LBB5_13
	v_and_b32_e32 v3, 15, v0
	v_lshl_or_b32 v1, v3, 2, 1
	v_lshrrev_b32_e32 v2, 4, v0
	v_mul_u32_u24_e32 v0, 40, v3
	v_mul_u32_u24_e32 v1, 10, v1
	v_add_lshl_u32 v0, v0, v2, 2
	v_add_lshl_u32 v1, v1, v2, 2
	v_add_u32_e32 v4, 0x50, v1
	v_mov_b32_e32 v8, v71
	v_mov_b32_e32 v9, v72
	v_mov_b32_e32 v10, v73
	v_mov_b32_e32 v11, v74
	v_lshlrev_b32_e32 v1, 4, v3
	ds_read_b128 v[4:7], v1 offset:9216
	v_mbcnt_lo_u32_b32 v0, -1, 0
	v_mbcnt_hi_u32_b32 v0, -1, v0
	v_and_b32_e32 v12, 64, v0
	v_xor_b32_e32 v1, 1, v0
	v_add_u32_e32 v12, 64, v12
	v_cmp_lt_i32_e32 vcc, v1, v12
	s_waitcnt vmcnt(3) lgkmcnt(0)
	v_fma_f32 v4, v4, v8, 0
	s_waitcnt vmcnt(2)
	v_fmac_f32_e32 v4, v5, v9
	v_cndmask_b32_e32 v1, v0, v1, vcc
	s_waitcnt vmcnt(1)
	v_fmac_f32_e32 v4, v6, v10
	v_lshlrev_b32_e32 v1, 2, v1
	s_waitcnt vmcnt(0)
	v_fmac_f32_e32 v4, v7, v11
	ds_bpermute_b32 v1, v1, v4
	v_xor_b32_e32 v5, 2, v0
	v_cmp_lt_i32_e32 vcc, v5, v12
	s_waitcnt lgkmcnt(0)
	v_add_f32_e32 v1, v4, v1
	v_cndmask_b32_e32 v5, v0, v5, vcc
	v_lshlrev_b32_e32 v5, 2, v5
	ds_bpermute_b32 v4, v5, v1
	v_xor_b32_e32 v5, 4, v0
	v_cmp_lt_i32_e32 vcc, v5, v12
	s_waitcnt lgkmcnt(0)
	v_add_f32_e32 v1, v1, v4
	v_cndmask_b32_e32 v5, v0, v5, vcc
	v_lshlrev_b32_e32 v5, 2, v5
	ds_bpermute_b32 v4, v5, v1
	v_xor_b32_e32 v5, 8, v0
	v_cmp_lt_i32_e32 vcc, v5, v12
	s_nop 1
	v_cndmask_b32_e32 v5, v0, v5, vcc
	s_waitcnt lgkmcnt(0)
	v_add_f32_e32 v0, v1, v4
	v_lshlrev_b32_e32 v1, 2, v5
	ds_bpermute_b32 v1, v1, v0
	v_cmp_eq_u32_e32 vcc, 0, v3
	s_and_b64 exec, exec, vcc
	s_cbranch_execz .LBB5_13
	v_mov_b32_e32 v3, v76
	s_waitcnt lgkmcnt(0)
	v_add_f32_e32 v4, v0, v1
	s_waitcnt vmcnt(0)
	v_mad_u64_u32 v[0:1], s[0:1], s2, 10, v[2:3]
	v_ashrrev_i32_e32 v1, 31, v0
	v_add_f32_e32 v2, v4, v3
	v_lshl_add_u64 v[0:1], v[0:1], 2, s[8:9]
	global_store_dword v[0:1], v2, off

	.amdhsa_kernel _Z10mlp_kernelPKfPKiS0_S0_S0_S0_S0_S0_Pf
		.amdhsa_group_segment_fixed_size 9472
		.amdhsa_private_segment_fixed_size 0
		.amdhsa_kernarg_size 72
		.amdhsa_user_sgpr_count 2
		.amdhsa_user_sgpr_dispatch_ptr 0
		.amdhsa_user_sgpr_queue_ptr 0
		.amdhsa_user_sgpr_kernarg_segment_ptr 1
		.amdhsa_user_sgpr_dispatch_id 0
		.amdhsa_user_sgpr_kernarg_preload_length 0
		.amdhsa_user_sgpr_kernarg_preload_offset 0
		.amdhsa_user_sgpr_private_segment_size 0
		.amdhsa_uses_dynamic_stack 0
		.amdhsa_enable_private_segment 0
		.amdhsa_system_sgpr_workgroup_id_x 1
		.amdhsa_system_sgpr_workgroup_id_y 0
		.amdhsa_system_sgpr_workgroup_id_z 0
		.amdhsa_system_sgpr_workgroup_info 0
		.amdhsa_system_vgpr_workitem_id 0
		.amdhsa_next_free_vgpr 77
		.amdhsa_next_free_sgpr 70
		.amdhsa_accum_offset 80
		.amdhsa_reserve_vcc 1
		.amdhsa_float_round_mode_32 0
		.amdhsa_float_round_mode_16_64 0
		.amdhsa_float_denorm_mode_32 3
		.amdhsa_float_denorm_mode_16_64 3
		.amdhsa_dx10_clamp 1
		.amdhsa_ieee_mode 1
		.amdhsa_fp16_overflow 0
		.amdhsa_tg_split 0
		.amdhsa_exception_fp_ieee_invalid_op 0
		.amdhsa_exception_fp_denorm_src 0
		.amdhsa_exception_fp_ieee_div_zero 0
		.amdhsa_exception_fp_ieee_overflow 0
		.amdhsa_exception_fp_ieee_underflow 0
		.amdhsa_exception_fp_ieee_inexact 0
		.amdhsa_exception_int_div_zero 0
	.end_amdhsa_kernel

amdhsa.kernels:
  - .agpr_count:     0
    .args:
      - .actual_access:  read_only
        .address_space:  global
        .offset:         0
        .size:           8
        .value_kind:     global_buffer
      - .actual_access:  read_only
        .address_space:  global
        .offset:         8
        .size:           8
        .value_kind:     global_buffer
      - .actual_access:  read_only
        .address_space:  global
        .offset:         16
        .size:           8
        .value_kind:     global_buffer
      - .actual_access:  read_only
        .address_space:  global
        .offset:         24
        .size:           8
        .value_kind:     global_buffer
      - .actual_access:  read_only
        .address_space:  global
        .offset:         32
        .size:           8
        .value_kind:     global_buffer
      - .actual_access:  read_only
        .address_space:  global
        .offset:         40
        .size:           8
        .value_kind:     global_buffer
      - .actual_access:  read_only
        .address_space:  global
        .offset:         48
        .size:           8
        .value_kind:     global_buffer
      - .actual_access:  read_only
        .address_space:  global
        .offset:         56
        .size:           8
        .value_kind:     global_buffer
      - .actual_access:  read_only
        .address_space:  global
        .offset:         64
        .size:           8
        .value_kind:     global_buffer
      - .actual_access:  read_only
        .address_space:  global
        .offset:         72
        .size:           8
        .value_kind:     global_buffer
      - .actual_access:  read_only
        .address_space:  global
        .offset:         80
        .size:           8
        .value_kind:     global_buffer
      - .actual_access:  read_only
        .address_space:  global
        .offset:         88
        .size:           8
        .value_kind:     global_buffer
      - .actual_access:  read_only
        .address_space:  global
        .offset:         96
        .size:           8
        .value_kind:     global_buffer
      - .actual_access:  write_only
        .address_space:  global
        .offset:         104
        .size:           8
        .value_kind:     global_buffer
      - .actual_access:  write_only
        .address_space:  global
        .offset:         112
        .size:           8
        .value_kind:     global_buffer
      - .actual_access:  write_only
        .address_space:  global
        .offset:         120
        .size:           8
        .value_kind:     global_buffer
      - .actual_access:  write_only
        .address_space:  global
        .offset:         128
        .size:           8
        .value_kind:     global_buffer
      - .actual_access:  write_only
        .address_space:  global
        .offset:         136
        .size:           8
        .value_kind:     global_buffer
      - .actual_access:  write_only
        .address_space:  global
        .offset:         144
        .size:           8
        .value_kind:     global_buffer
      - .actual_access:  write_only
        .address_space:  global
        .offset:         152
        .size:           8
        .value_kind:     global_buffer
      - .actual_access:  write_only
        .address_space:  global
        .offset:         160
        .size:           8
        .value_kind:     global_buffer
      - .actual_access:  write_only
        .address_space:  global
        .offset:         168
        .size:           8
        .value_kind:     global_buffer
      - .actual_access:  read_only
        .address_space:  global
        .offset:         176
        .size:           8
        .value_kind:     global_buffer
    .group_segment_fixed_size: 29696
    .kernarg_segment_align: 8
    .kernarg_segment_size: 184
    .language:       OpenCL C
    .language_version:
      - 2
      - 0
    .max_flat_workgroup_size: 512
    .name:           _Z12front_kernelPKiS0_PKfS2_S2_S2_S2_S2_S2_S2_S2_S2_S2_PjS3_PiS4_PDF16_PfS6_S4_S5_S0_
    .private_segment_fixed_size: 0
    .sgpr_count:     30
    .sgpr_spill_count: 0
    .symbol:         _Z12front_kernelPKiS0_PKfS2_S2_S2_S2_S2_S2_S2_S2_S2_S2_PjS3_PiS4_PDF16_PfS6_S4_S5_S0_.kd
    .uniform_work_group_size: 1
    .uses_dynamic_stack: false
    .vgpr_count:     80
    .vgpr_spill_count: 0
    .wavefront_size: 64
  - .agpr_count:     0
    .args:
      - .actual_access:  read_only
        .address_space:  global
        .offset:         0
        .size:           8
        .value_kind:     global_buffer
      - .actual_access:  read_only
        .address_space:  global
        .offset:         8
        .size:           8
        .value_kind:     global_buffer
      - .actual_access:  write_only
        .address_space:  global
        .offset:         16
        .size:           8
        .value_kind:     global_buffer
      - .actual_access:  write_only
        .address_space:  global
        .offset:         24
        .size:           8
        .value_kind:     global_buffer
      - .actual_access:  write_only
        .address_space:  global
        .offset:         32
        .size:           8
        .value_kind:     global_buffer
      - .actual_access:  read_only
        .address_space:  global
        .offset:         40
        .size:           8
        .value_kind:     global_buffer
      - .actual_access:  read_only
        .address_space:  global
        .offset:         48
        .size:           8
        .value_kind:     global_buffer
      - .actual_access:  write_only
        .address_space:  global
        .offset:         56
        .size:           8
        .value_kind:     global_buffer
      - .actual_access:  write_only
        .address_space:  global
        .offset:         64
        .size:           8
        .value_kind:     global_buffer
    .group_segment_fixed_size: 40960
    .kernarg_segment_align: 8
    .kernarg_segment_size: 72
    .language:       OpenCL C
    .language_version:
      - 2
      - 0
    .max_flat_workgroup_size: 512
    .name:           _Z13second_kernelPKfPKDF16_PDF16_PfS4_PKjPKiPiS9_
    .private_segment_fixed_size: 0
    .sgpr_count:     29
    .sgpr_spill_count: 0
    .symbol:         _Z13second_kernelPKfPKDF16_PDF16_PfS4_PKjPKiPiS9_.kd
    .uniform_work_group_size: 1
    .uses_dynamic_stack: false
    .vgpr_count:     64
    .vgpr_spill_count: 0
    .wavefront_size: 64
  - .agpr_count:     0
    .args:
      - .actual_access:  read_only
        .address_space:  global
        .offset:         0
        .size:           8
        .value_kind:     global_buffer
      - .actual_access:  read_only
        .address_space:  global
        .offset:         8
        .size:           8
        .value_kind:     global_buffer
      - .actual_access:  read_only
        .address_space:  global
        .offset:         16
        .size:           8
        .value_kind:     global_buffer
      - .actual_access:  read_only
        .address_space:  global
        .offset:         24
        .size:           8
        .value_kind:     global_buffer
      - .actual_access:  read_only
        .address_space:  global
        .offset:         32
        .size:           8
        .value_kind:     global_buffer
      - .actual_access:  read_only
        .address_space:  global
        .offset:         40
        .size:           8
        .value_kind:     global_buffer
      - .actual_access:  read_only
        .address_space:  global
        .offset:         48
        .size:           8
        .value_kind:     global_buffer
      - .actual_access:  write_only
        .address_space:  global
        .offset:         56
        .size:           8
        .value_kind:     global_buffer
      - .actual_access:  write_only
        .address_space:  global
        .offset:         64
        .size:           8
        .value_kind:     global_buffer
      - .actual_access:  write_only
        .address_space:  global
        .offset:         72
        .size:           8
        .value_kind:     global_buffer
      - .offset:         80
        .size:           4
        .value_kind:     by_value
    .group_segment_fixed_size: 10240
    .kernarg_segment_align: 8
    .kernarg_segment_size: 84
    .language:       OpenCL C
    .language_version:
      - 2
      - 0
    .max_flat_workgroup_size: 256
    .name:           _Z11agg1_kernelPKDF16_PKfS2_PKiS4_S2_S2_PDF16_PfS6_i
    .private_segment_fixed_size: 0
    .sgpr_count:     50
    .sgpr_spill_count: 0
    .symbol:         _Z11agg1_kernelPKDF16_PKfS2_PKiS4_S2_S2_PDF16_PfS6_i.kd
    .uniform_work_group_size: 1
    .uses_dynamic_stack: false
    .vgpr_count:     70
    .vgpr_spill_count: 0
    .wavefront_size: 64
  - .agpr_count:     0
    .args:
      - .actual_access:  read_only
        .address_space:  global
        .offset:         0
        .size:           8
        .value_kind:     global_buffer
      - .actual_access:  read_only
        .address_space:  global
        .offset:         8
        .size:           8
        .value_kind:     global_buffer
      - .actual_access:  read_only
        .address_space:  global
        .offset:         16
        .size:           8
        .value_kind:     global_buffer
      - .actual_access:  read_only
        .address_space:  global
        .offset:         24
        .size:           8
        .value_kind:     global_buffer
      - .actual_access:  read_only
        .address_space:  global
        .offset:         32
        .size:           8
        .value_kind:     global_buffer
      - .actual_access:  write_only
        .address_space:  global
        .offset:         40
        .size:           8
        .value_kind:     global_buffer
      - .offset:         48
        .size:           4
        .value_kind:     by_value
    .group_segment_fixed_size: 0
    .kernarg_segment_align: 8
    .kernarg_segment_size: 52
    .language:       OpenCL C
    .language_version:
      - 2
      - 0
    .max_flat_workgroup_size: 256
    .name:           _Z13stats2_kernelPKiS0_PKfS2_S0_P15HIP_vector_typeIfLj4EEi
    .private_segment_fixed_size: 0
    .sgpr_count:     27
    .sgpr_spill_count: 0
    .symbol:         _Z13stats2_kernelPKiS0_PKfS2_S0_P15HIP_vector_typeIfLj4EEi.kd
    .uniform_work_group_size: 1
    .uses_dynamic_stack: false
    .vgpr_count:     32
    .vgpr_spill_count: 0
    .wavefront_size: 64
  - .agpr_count:     0
    .args:
      - .actual_access:  read_only
        .address_space:  global
        .offset:         0
        .size:           8
        .value_kind:     global_buffer
      - .actual_access:  read_only
        .address_space:  global
        .offset:         8
        .size:           8
        .value_kind:     global_buffer
      - .actual_access:  read_only
        .address_space:  global
        .offset:         16
        .size:           8
        .value_kind:     global_buffer
      - .actual_access:  read_only
        .address_space:  global
        .offset:         24
        .size:           8
        .value_kind:     global_buffer
      - .actual_access:  read_only
        .address_space:  global
        .offset:         32
        .size:           8
        .value_kind:     global_buffer
      - .actual_access:  write_only
        .address_space:  global
        .offset:         40
        .size:           8
        .value_kind:     global_buffer
      - .offset:         48
        .size:           4
        .value_kind:     by_value
    .group_segment_fixed_size: 69728
    .kernarg_segment_align: 8
    .kernarg_segment_size: 52
    .language:       OpenCL C
    .language_version:
      - 2
      - 0
    .max_flat_workgroup_size: 1024
    .name:           _Z12pool2_kernelPKjPKiPKfPK15HIP_vector_typeIfLj4EEPKDF16_Pfi
    .private_segment_fixed_size: 0
    .sgpr_count:     26
    .sgpr_spill_count: 0
    .symbol:         _Z12pool2_kernelPKjPKiPKfPK15HIP_vector_typeIfLj4EEPKDF16_Pfi.kd
    .uniform_work_group_size: 1
    .uses_dynamic_stack: false
    .vgpr_count:     128
    .vgpr_spill_count: 0
    .wavefront_size: 64
  - .agpr_count:     0
    .args:
      - .actual_access:  read_only
        .address_space:  global
        .offset:         0
        .size:           8
        .value_kind:     global_buffer
      - .actual_access:  read_only
        .address_space:  global
        .offset:         8
        .size:           8
        .value_kind:     global_buffer
      - .actual_access:  read_only
        .address_space:  global
        .offset:         16
        .size:           8
        .value_kind:     global_buffer
      - .actual_access:  read_only
        .address_space:  global
        .offset:         24
        .size:           8
        .value_kind:     global_buffer
      - .actual_access:  read_only
        .address_space:  global
        .offset:         32
        .size:           8
        .value_kind:     global_buffer
      - .actual_access:  read_only
        .address_space:  global
        .offset:         40
        .size:           8
        .value_kind:     global_buffer
      - .actual_access:  read_only
        .address_space:  global
        .offset:         48
        .size:           8
        .value_kind:     global_buffer
      - .actual_access:  read_only
        .address_space:  global
        .offset:         56
        .size:           8
        .value_kind:     global_buffer
      - .actual_access:  write_only
        .address_space:  global
        .offset:         64
        .size:           8
        .value_kind:     global_buffer
    .group_segment_fixed_size: 9472
    .kernarg_segment_align: 8
    .kernarg_segment_size: 72
    .language:       OpenCL C
    .language_version:
      - 2
      - 0
    .max_flat_workgroup_size: 1024
    .name:           _Z10mlp_kernelPKfPKiS0_S0_S0_S0_S0_S0_Pf
    .private_segment_fixed_size: 0
    .sgpr_count:     76
    .sgpr_spill_count: 0
    .symbol:         _Z10mlp_kernelPKfPKiS0_S0_S0_S0_S0_S0_Pf.kd
    .uniform_work_group_size: 1
    .uses_dynamic_stack: false
    .vgpr_count:     77
    .vgpr_spill_count: 0
    .wavefront_size: 64
